# MoE: epilogue bias vectors preloaded at unit start into spare VGPRs (constants restored at phase exit), epilogue load latency removed
# speedup vs baseline: 1.0187x; 1.0048x over previous
.LBB0_2060:
	s_mov_b32 s88, s12
	s_ashr_i32 s89, s12, 31
	v_mov_b32_e32 v189, 1
	v_mov_b32_e32 v139, 0
	s_cmp_gt_i32 s60, 7
	s_cbranch_scc1 .Lbp_down
	s_lshl_b64 s[88:89], s[88:89], 13
	s_add_u32 s88, s72, s88
	s_addc_u32 s89, s73, s89
	v_lshl_or_b32 v138, s60, 7, v178
	s_mov_b64 s[90:91], 0x1000
	v_lshl_add_u64 v[138:139], v[138:139], 2, s[88:89]
	v_lshl_add_u64 v[140:141], v[138:139], 0, s[90:91]
	global_load_dwordx4 v[206:209], v[138:139], off offset:16
	global_load_dwordx4 v[34:37], v[138:139], off
	global_load_dwordx4 v[212:215], v[140:141], off
	global_load_dwordx2 v[216:217], v[140:141], off offset:16
	global_load_dwordx2 v[204:205], v[140:141], off offset:24
	s_branch .Lbp_done
.Lbp_down:
	s_lshl_b64 s[88:89], s[88:89], 12
	s_add_u32 s88, s74, s88
	s_addc_u32 s89, s75, s89
	v_lshl_add_u32 v138, s60, 8, v179
	s_nop 0
	v_lshl_add_u64 v[138:139], v[138:139], 2, s[88:89]
	global_load_dwordx4 v[34:37], v[138:139], off offset:16
	global_load_dwordx4 v[212:215], v[138:139], off
	global_load_dwordx4 v[206:209], v[138:139], off offset:528
	global_load_dwordx2 v[216:217], v[138:139], off offset:512
	global_load_dwordx2 v[204:205], v[138:139], off offset:520
.Lbp_done:
	s_and_b64 s[2:3], s[54:55], exec
	v_readlane_b32 s84, v252, 29
	s_cselect_b32 s3, s65, s66
	s_cselect_b32 s2, s11, s84
	s_add_u32 s29, s52, 0x100
	s_addc_u32 s31, s53, 0
	s_add_u32 s40, s34, 0x80
	v_mov_b32_e32 v155, v1
	v_mov_b32_e32 v161, v1
	s_addc_u32 s41, s35, 0
	v_lshl_add_u64 v[134:135], s[40:41], 0, v[160:161]
	v_lshl_add_u64 v[136:137], s[40:41], 0, v[154:155]
	s_mov_b32 s13, -2
	s_mov_b64 s[52:53], 0
	v_mov_b32_e32 v0, s50
	v_readlane_b32 s85, v252, 30
	v_readlane_b32 s86, v252, 31
	v_readlane_b32 s87, v252, 32
	s_cmpk_lg_i32 s52, 0x200
	s_cselect_b64 s[40:41], -1, 0
	v_cmp_gt_i32_e32 vcc, 0, v0
	s_or_b64 vcc, s[40:41], vcc
	s_nor_b64 s[40:41], s[6:7], vcc
	v_cndmask_b32_e32 v138, -1, v0, vcc
	s_and_saveexec_b64 s[50:51], s[40:41]
	s_cbranch_execz .Lpk_2063
	v_lshl_add_u64 v[138:139], v[0:1], 2, s[14:15]
	global_atomic_add v[138:139], v189, off
	v_mov_b32_e32 v138, -1

.LBB0_2061:
	s_cmpk_lg_i32 s52, 0x200
	s_cselect_b64 s[40:41], -1, 0
	v_cmp_gt_i32_e32 vcc, 0, v0
	s_or_b64 vcc, s[40:41], vcc
	s_nor_b64 s[40:41], s[6:7], vcc
	v_cndmask_b32_e32 v138, -1, v0, vcc
	s_and_saveexec_b64 s[50:51], s[40:41]
	s_cbranch_execz .LBB0_2063
	v_lshl_add_u64 v[138:139], v[0:1], 2, s[14:15]
	global_atomic_add v[138:139], v189, off
	v_mov_b32_e32 v138, -1

.LBB0_2073:
	s_mov_b32 s32, 1
	v_lshl_add_u32 v0, s60, 8, v179
	v_ashrrev_i32_e32 v163, 31, v162
	v_lshlrev_b64 v[164:165], 11, v[162:163]
	v_lshl_add_u64 v[164:165], s[20:21], 0, v[164:165]
	v_lshlrev_b64 v[166:167], 1, v[0:1]
	v_lshl_add_u64 v[164:165], v[164:165], 0, v[166:167]
	s_mov_b32 s33, 0x40000
	s_mov_b64 s[40:41], 0x40000
	v_mov_b64_e32 v[134:135], v[206:207]
	v_mov_b64_e32 v[136:137], v[208:209]
	v_mov_b64_e32 v[142:143], v[34:35]
	v_mov_b64_e32 v[144:145], v[36:37]
	v_mov_b64_e32 v[146:147], v[212:213]
	v_mov_b64_e32 v[148:149], v[214:215]
	v_mov_b64_e32 v[138:139], v[216:217]
	v_mov_b64_e32 v[140:141], v[204:205]
	s_waitcnt vmcnt(0)
	v_pk_add_f32 v[172:173], v[128:129], v[144:145]
	v_pk_add_f32 v[170:171], v[132:133], v[148:149]
	v_pk_add_f32 v[168:169], v[130:131], v[146:147]
	v_pk_add_f32 v[182:183], v[126:127], v[142:143]
	v_cvt_pk_bf16_f32 v168, v168, v169
	v_cvt_pk_bf16_f32 v169, v170, v171
	v_cvt_pk_bf16_f32 v170, v182, v183
	v_cvt_pk_bf16_f32 v171, v172, v173
	global_store_dwordx4 v[164:165], v[168:171], off
	v_pk_add_f32 v[172:173], v[96:97], v[136:137]
	v_pk_add_f32 v[182:183], v[94:95], v[134:135]
	v_pk_add_f32 v[170:171], v[100:101], v[140:141]
	v_pk_add_f32 v[168:169], v[98:99], v[138:139]
	v_pk_add_f32 v[184:185], v[118:119], v[142:143]
	v_cvt_pk_bf16_f32 v168, v168, v169
	v_cvt_pk_bf16_f32 v169, v170, v171
	v_cvt_pk_bf16_f32 v170, v182, v183
	v_cvt_pk_bf16_f32 v171, v172, v173
	global_store_dwordx4 v[164:165], v[168:171], off offset:256
	v_pk_add_f32 v[182:183], v[120:121], v[144:145]
	s_nop 0
	v_or_b32_e32 v168, 16, v162
	v_ashrrev_i32_e32 v169, 31, v168
	v_lshlrev_b64 v[168:169], 11, v[168:169]
	v_lshl_add_u64 v[168:169], s[20:21], 0, v[168:169]
	v_lshl_add_u64 v[172:173], v[168:169], 0, v[166:167]
	v_pk_add_f32 v[170:171], v[124:125], v[148:149]
	v_pk_add_f32 v[168:169], v[122:123], v[146:147]
	s_nop 0
	v_cvt_pk_bf16_f32 v168, v168, v169
	v_cvt_pk_bf16_f32 v169, v170, v171
	v_cvt_pk_bf16_f32 v170, v184, v185
	v_cvt_pk_bf16_f32 v171, v182, v183
	global_store_dwordx4 v[172:173], v[168:171], off
	v_pk_add_f32 v[182:183], v[88:89], v[136:137]
	v_pk_add_f32 v[184:185], v[86:87], v[134:135]
	v_pk_add_f32 v[170:171], v[92:93], v[140:141]
	v_pk_add_f32 v[168:169], v[90:91], v[138:139]
	s_nop 0
	v_cvt_pk_bf16_f32 v168, v168, v169
	v_cvt_pk_bf16_f32 v169, v170, v171
	v_cvt_pk_bf16_f32 v170, v184, v185
	v_cvt_pk_bf16_f32 v171, v182, v183
	global_store_dwordx4 v[172:173], v[168:171], off offset:256
	v_pk_add_f32 v[182:183], v[112:113], v[144:145]
	v_pk_add_f32 v[184:185], v[110:111], v[142:143]
	v_or_b32_e32 v168, 32, v162
	v_ashrrev_i32_e32 v169, 31, v168
	v_lshlrev_b64 v[168:169], 11, v[168:169]
	v_lshl_add_u64 v[168:169], s[20:21], 0, v[168:169]
	v_lshl_add_u64 v[172:173], v[168:169], 0, v[166:167]
	v_pk_add_f32 v[170:171], v[116:117], v[148:149]
	v_pk_add_f32 v[168:169], v[114:115], v[146:147]
	s_nop 0
	v_cvt_pk_bf16_f32 v168, v168, v169
	v_cvt_pk_bf16_f32 v169, v170, v171
	v_cvt_pk_bf16_f32 v170, v184, v185
	v_cvt_pk_bf16_f32 v171, v182, v183
	global_store_dwordx4 v[172:173], v[168:171], off
	v_pk_add_f32 v[182:183], v[80:81], v[136:137]
	v_pk_add_f32 v[184:185], v[78:79], v[134:135]
	v_pk_add_f32 v[170:171], v[84:85], v[140:141]
	v_pk_add_f32 v[168:169], v[82:83], v[138:139]
	s_nop 0
	v_cvt_pk_bf16_f32 v168, v168, v169
	v_cvt_pk_bf16_f32 v169, v170, v171
	v_cvt_pk_bf16_f32 v170, v184, v185
	v_cvt_pk_bf16_f32 v171, v182, v183
	global_store_dwordx4 v[172:173], v[168:171], off offset:256
	v_pk_add_f32 v[172:173], v[104:105], v[144:145]
	v_pk_add_f32 v[182:183], v[102:103], v[142:143]
	v_or_b32_e32 v168, 48, v162
	v_ashrrev_i32_e32 v169, 31, v168
	v_lshlrev_b64 v[168:169], 11, v[168:169]
	v_lshl_add_u64 v[168:169], s[20:21], 0, v[168:169]
	v_lshl_add_u64 v[170:171], v[168:169], 0, v[166:167]
	v_pk_add_f32 v[168:169], v[108:109], v[148:149]
	v_pk_add_f32 v[166:167], v[106:107], v[146:147]
	s_nop 0
	v_cvt_pk_bf16_f32 v166, v166, v167
	v_cvt_pk_bf16_f32 v167, v168, v169
	v_cvt_pk_bf16_f32 v168, v182, v183
	v_cvt_pk_bf16_f32 v169, v172, v173
	global_store_dwordx4 v[170:171], v[166:169], off
	v_pk_add_f32 v[172:173], v[72:73], v[136:137]
	v_pk_add_f32 v[182:183], v[70:71], v[134:135]
	v_pk_add_f32 v[168:169], v[76:77], v[140:141]
	v_pk_add_f32 v[166:167], v[74:75], v[138:139]
	s_nop 0
	v_cvt_pk_bf16_f32 v166, v166, v167
	v_cvt_pk_bf16_f32 v167, v168, v169
	v_cvt_pk_bf16_f32 v168, v182, v183
	v_cvt_pk_bf16_f32 v169, v172, v173
	global_store_dwordx4 v[170:171], v[166:169], off offset:256
	v_pk_add_f32 v[172:173], v[64:65], v[144:145]
	v_pk_add_f32 v[182:183], v[62:63], v[142:143]
	v_pk_add_f32 v[168:169], v[68:69], v[148:149]
	v_pk_add_f32 v[166:167], v[66:67], v[146:147]
	v_lshl_add_u64 v[170:171], v[164:165], 0, s[40:41]
	v_cvt_pk_bf16_f32 v166, v166, v167
	v_cvt_pk_bf16_f32 v167, v168, v169
	v_cvt_pk_bf16_f32 v169, v172, v173
	v_add_co_u32_e32 v172, vcc, s33, v164
	v_cvt_pk_bf16_f32 v168, v182, v183
	s_nop 0
	v_addc_co_u32_e32 v173, vcc, 0, v165, vcc
	global_store_dwordx4 v[172:173], v[166:169], off
	v_pk_add_f32 v[172:173], v[28:29], v[136:137]
	v_pk_add_f32 v[182:183], v[26:27], v[134:135]
	v_pk_add_f32 v[168:169], v[32:33], v[140:141]
	v_pk_add_f32 v[166:167], v[30:31], v[138:139]
	s_mov_b32 s33, 0x48000
	v_cvt_pk_bf16_f32 v166, v166, v167
	v_cvt_pk_bf16_f32 v167, v168, v169
	v_cvt_pk_bf16_f32 v168, v182, v183
	v_cvt_pk_bf16_f32 v169, v172, v173
	global_store_dwordx4 v[170:171], v[166:169], off offset:256
	v_pk_add_f32 v[172:173], v[56:57], v[144:145]
	v_pk_add_f32 v[182:183], v[54:55], v[142:143]
	v_pk_add_f32 v[168:169], v[60:61], v[148:149]
	v_pk_add_f32 v[166:167], v[58:59], v[146:147]
	s_mov_b64 s[40:41], 0x48000
	v_cvt_pk_bf16_f32 v166, v166, v167
	v_cvt_pk_bf16_f32 v167, v168, v169
	v_cvt_pk_bf16_f32 v169, v172, v173
	v_add_co_u32_e32 v172, vcc, s33, v164
	v_cvt_pk_bf16_f32 v168, v182, v183
	s_nop 0
	v_addc_co_u32_e32 v173, vcc, 0, v165, vcc
	global_store_dwordx4 v[172:173], v[166:169], off
	v_pk_add_f32 v[172:173], v[20:21], v[136:137]
	v_pk_add_f32 v[182:183], v[18:19], v[134:135]
	v_pk_add_f32 v[168:169], v[24:25], v[140:141]
	v_pk_add_f32 v[166:167], v[22:23], v[138:139]
	v_lshl_add_u64 v[170:171], v[164:165], 0, s[40:41]
	v_cvt_pk_bf16_f32 v166, v166, v167
	v_cvt_pk_bf16_f32 v167, v168, v169
	v_cvt_pk_bf16_f32 v168, v182, v183
	v_cvt_pk_bf16_f32 v169, v172, v173
	global_store_dwordx4 v[170:171], v[166:169], off offset:256
	v_pk_add_f32 v[172:173], v[48:49], v[144:145]
	s_mov_b32 s33, 0x50000
	v_pk_add_f32 v[168:169], v[52:53], v[148:149]
	v_pk_add_f32 v[166:167], v[50:51], v[146:147]
	v_pk_add_f32 v[182:183], v[46:47], v[142:143]
	v_cvt_pk_bf16_f32 v166, v166, v167
	v_cvt_pk_bf16_f32 v167, v168, v169
	v_cvt_pk_bf16_f32 v169, v172, v173
	v_add_co_u32_e32 v172, vcc, s33, v164
	v_cvt_pk_bf16_f32 v168, v182, v183
	s_nop 0
	v_addc_co_u32_e32 v173, vcc, 0, v165, vcc
	s_mov_b64 s[40:41], 0x50000
	global_store_dwordx4 v[172:173], v[166:169], off
	v_pk_add_f32 v[172:173], v[12:13], v[136:137]
	v_pk_add_f32 v[182:183], v[10:11], v[134:135]
	v_pk_add_f32 v[168:169], v[16:17], v[140:141]
	v_pk_add_f32 v[166:167], v[14:15], v[138:139]
	v_lshl_add_u64 v[170:171], v[164:165], 0, s[40:41]
	v_cvt_pk_bf16_f32 v166, v166, v167
	v_cvt_pk_bf16_f32 v167, v168, v169
	v_cvt_pk_bf16_f32 v168, v182, v183
	v_cvt_pk_bf16_f32 v169, v172, v173
	v_pk_add_f32 v[146:147], v[42:43], v[146:147]
	s_mov_b32 s33, 0x58000
	global_store_dwordx4 v[170:171], v[166:169], off offset:256
	v_pk_add_f32 v[148:149], v[44:45], v[148:149]
	s_mov_b64 s[40:41], 0x58000
	v_pk_add_f32 v[168:169], v[40:41], v[144:145]
	v_pk_add_f32 v[144:145], v[38:39], v[142:143]
	v_cvt_pk_bf16_f32 v142, v146, v147
	v_add_co_u32_e32 v146, vcc, s33, v164
	v_cvt_pk_bf16_f32 v143, v148, v149
	v_cvt_pk_bf16_f32 v144, v144, v145
	v_cvt_pk_bf16_f32 v145, v168, v169
	v_addc_co_u32_e32 v147, vcc, 0, v165, vcc
	global_store_dwordx4 v[146:147], v[142:145], off
	v_pk_add_f32 v[140:141], v[8:9], v[140:141]
	v_pk_add_f32 v[138:139], v[6:7], v[138:139]
	v_pk_add_f32 v[142:143], v[4:5], v[136:137]
	v_pk_add_f32 v[136:137], v[2:3], v[134:135]
	v_lshl_add_u64 v[166:167], v[164:165], 0, s[40:41]
	v_cvt_pk_bf16_f32 v134, v138, v139
	v_cvt_pk_bf16_f32 v135, v140, v141
	v_cvt_pk_bf16_f32 v136, v136, v137
	v_cvt_pk_bf16_f32 v137, v142, v143
	global_store_dwordx4 v[166:167], v[134:137], off offset:256
	s_mov_b32 s50, -1
	s_cbranch_execnz .LBB0_2069
.LBB0_2074:
	s_mov_b32 s32, 1
	v_lshl_or_b32 v0, s60, 7, v178
	s_mov_b32 s13, 0xc0e00000
	v_lshlrev_b32_e32 v0, 1, v0
	v_lshl_add_u32 v0, v162, 11, v0
	v_readlane_b32 s40, v252, 29
	v_readlane_b32 s41, v252, 30
	v_readlane_b32 s42, v252, 31
	v_readlane_b32 s43, v252, 32
	s_mov_b32 s50, s10
	v_mov_b64_e32 v[134:135], v[206:207]
	v_mov_b64_e32 v[136:137], v[208:209]
	v_mov_b64_e32 v[142:143], v[34:35]
	v_mov_b64_e32 v[144:145], v[36:37]
	v_mov_b64_e32 v[146:147], v[212:213]
	v_mov_b64_e32 v[148:149], v[214:215]
	v_mov_b64_e32 v[138:139], v[216:217]
	v_mov_b64_e32 v[140:141], v[204:205]
	v_add_f32_e32 v155, v130, v142
	v_min_f32_e32 v164, 0x40e00000, v155
	v_mul_f32_e32 v155, 0xbfd9db23, v164
	v_mul_f32_e32 v155, 0x3fb8aa3b, v155
	v_exp_f32_e32 v155, v155
	v_add_f32_e32 v161, v98, v146
	v_add_f32_e32 v155, 1.0, v155
	v_rcp_f32_e32 v168, v155
	v_add_f32_e32 v155, v131, v143
	v_min_f32_e32 v165, 0x40e00000, v155
	v_mul_f32_e32 v155, 0xbfd9db23, v165
	v_mul_f32_e32 v155, 0x3fb8aa3b, v155
	v_exp_f32_e32 v155, v155
	v_med3_f32 v166, v161, s13, v222
	v_add_f32_e32 v161, v99, v147
	v_med3_f32 v167, v161, s13, v222
	v_add_f32_e32 v155, 1.0, v155
	v_rcp_f32_e32 v169, v155
	v_pk_add_f32 v[166:167], v[166:167], 1.0 op_sel_hi:[1,0]
	v_add_f32_e32 v155, v132, v144
	v_add_f32_e32 v161, v100, v148
	v_pk_mul_f32 v[164:165], v[164:165], v[168:169]
	v_med3_f32 v168, v161, s13, v222
	v_pk_mul_f32 v[164:165], v[166:167], v[164:165]
	v_min_f32_e32 v166, 0x40e00000, v155
	v_mul_f32_e32 v155, 0xbfd9db23, v166
	v_mul_f32_e32 v155, 0x3fb8aa3b, v155
	v_exp_f32_e32 v155, v155
	v_add_f32_e32 v161, v101, v149
	v_med3_f32 v169, v161, s13, v222
	v_pk_add_f32 v[168:169], v[168:169], 1.0 op_sel_hi:[1,0]
	v_add_f32_e32 v155, 1.0, v155
	v_rcp_f32_e32 v170, v155
	v_add_f32_e32 v155, v133, v145
	v_min_f32_e32 v167, 0x40e00000, v155
	v_mul_f32_e32 v155, 0xbfd9db23, v167
	v_mul_f32_e32 v155, 0x3fb8aa3b, v155
	v_exp_f32_e32 v155, v155
	v_add_f32_e32 v161, v94, v138
	v_cvt_pk_bf16_f32 v164, v164, v165
	v_add_f32_e32 v155, 1.0, v155
	v_rcp_f32_e32 v171, v155
	v_add_f32_e32 v155, v126, v134
	v_pk_mul_f32 v[166:167], v[166:167], v[170:171]
	s_nop 0
	v_pk_mul_f32 v[166:167], v[168:169], v[166:167]
	v_min_f32_e32 v168, 0x40e00000, v155
	v_mul_f32_e32 v155, 0xbfd9db23, v168
	v_mul_f32_e32 v155, 0x3fb8aa3b, v155
	v_exp_f32_e32 v155, v155
	v_med3_f32 v170, v161, s13, v222
	v_add_f32_e32 v161, v95, v139
	v_med3_f32 v171, v161, s13, v222
	v_add_f32_e32 v155, 1.0, v155
	v_rcp_f32_e32 v172, v155
	v_add_f32_e32 v155, v127, v135
	v_min_f32_e32 v169, 0x40e00000, v155
	v_mul_f32_e32 v155, 0xbfd9db23, v169
	v_mul_f32_e32 v155, 0x3fb8aa3b, v155
	v_exp_f32_e32 v155, v155
	v_pk_add_f32 v[170:171], v[170:171], 1.0 op_sel_hi:[1,0]
	v_add_f32_e32 v161, v96, v140
	v_med3_f32 v182, v161, s13, v222
	v_add_f32_e32 v155, 1.0, v155
	v_rcp_f32_e32 v173, v155
	v_add_f32_e32 v155, v128, v136
	v_add_f32_e32 v161, v97, v141
	v_med3_f32 v183, v161, s13, v222
	v_pk_mul_f32 v[168:169], v[168:169], v[172:173]
	v_pk_add_f32 v[182:183], v[182:183], 1.0 op_sel_hi:[1,0]
	v_pk_mul_f32 v[168:169], v[170:171], v[168:169]
	v_min_f32_e32 v170, 0x40e00000, v155
	v_mul_f32_e32 v155, 0xbfd9db23, v170
	v_mul_f32_e32 v155, 0x3fb8aa3b, v155
	v_exp_f32_e32 v155, v155
	v_cvt_pk_bf16_f32 v165, v166, v167
	v_cvt_pk_bf16_f32 v166, v168, v169
	v_add_f32_e32 v161, v90, v146
	v_add_f32_e32 v155, 1.0, v155
	v_rcp_f32_e32 v172, v155
	v_add_f32_e32 v155, v129, v137
	v_min_f32_e32 v171, 0x40e00000, v155
	v_mul_f32_e32 v155, 0xbfd9db23, v171
	v_mul_f32_e32 v155, 0x3fb8aa3b, v155
	v_exp_f32_e32 v155, v155
	s_nop 0
	v_add_f32_e32 v155, 1.0, v155
	v_rcp_f32_e32 v173, v155
	v_add_f32_e32 v155, v122, v142
	v_min_f32_e32 v162, 0x40e00000, v155
	v_mul_f32_e32 v155, 0xbfd9db23, v162
	v_mul_f32_e32 v155, 0x3fb8aa3b, v155
	v_exp_f32_e32 v155, v155
	v_pk_mul_f32 v[170:171], v[170:171], v[172:173]
	v_add_f32_e32 v155, 1.0, v155
	v_pk_mul_f32 v[170:171], v[182:183], v[170:171]
	s_nop 0
	v_cvt_pk_bf16_f32 v167, v170, v171
	s_waitcnt vmcnt(0)
	buffer_store_dwordx4 v[164:167], v0, s[40:43], 0 offen sc1
	s_nop 1
	v_rcp_f32_e32 v166, v155
	v_add_f32_e32 v155, v123, v143
	v_min_f32_e32 v163, 0x40e00000, v155
	v_mul_f32_e32 v155, 0xbfd9db23, v163
	v_mul_f32_e32 v155, 0x3fb8aa3b, v155
	v_exp_f32_e32 v155, v155
	v_med3_f32 v164, v161, s13, v222
	v_add_f32_e32 v161, v91, v147
	v_med3_f32 v165, v161, s13, v222
	v_add_f32_e32 v155, 1.0, v155
	v_rcp_f32_e32 v167, v155
	v_pk_add_f32 v[164:165], v[164:165], 1.0 op_sel_hi:[1,0]
	v_add_f32_e32 v155, v124, v144
	v_add_f32_e32 v161, v92, v148
	v_pk_mul_f32 v[162:163], v[162:163], v[166:167]
	v_med3_f32 v166, v161, s13, v222
	v_pk_mul_f32 v[162:163], v[164:165], v[162:163]
	v_min_f32_e32 v164, 0x40e00000, v155
	v_mul_f32_e32 v155, 0xbfd9db23, v164
	v_mul_f32_e32 v155, 0x3fb8aa3b, v155
	v_exp_f32_e32 v155, v155
	v_add_f32_e32 v161, v93, v149
	v_med3_f32 v167, v161, s13, v222
	v_pk_add_f32 v[166:167], v[166:167], 1.0 op_sel_hi:[1,0]
	v_add_f32_e32 v155, 1.0, v155
	v_rcp_f32_e32 v168, v155
	v_add_f32_e32 v155, v125, v145
	v_min_f32_e32 v165, 0x40e00000, v155
	v_mul_f32_e32 v155, 0xbfd9db23, v165
	v_mul_f32_e32 v155, 0x3fb8aa3b, v155
	v_exp_f32_e32 v155, v155
	v_add_f32_e32 v161, v86, v138
	v_cvt_pk_bf16_f32 v162, v162, v163
	v_add_f32_e32 v155, 1.0, v155
	v_rcp_f32_e32 v169, v155
	v_add_f32_e32 v155, v118, v134
	v_pk_mul_f32 v[164:165], v[164:165], v[168:169]
	s_nop 0
	v_pk_mul_f32 v[164:165], v[166:167], v[164:165]
	v_min_f32_e32 v166, 0x40e00000, v155
	v_mul_f32_e32 v155, 0xbfd9db23, v166
	v_mul_f32_e32 v155, 0x3fb8aa3b, v155
	v_exp_f32_e32 v155, v155
	v_med3_f32 v168, v161, s13, v222
	v_add_f32_e32 v161, v87, v139
	v_med3_f32 v169, v161, s13, v222
	v_add_f32_e32 v155, 1.0, v155
	v_rcp_f32_e32 v170, v155
	v_add_f32_e32 v155, v119, v135
	v_min_f32_e32 v167, 0x40e00000, v155
	v_mul_f32_e32 v155, 0xbfd9db23, v167
	v_mul_f32_e32 v155, 0x3fb8aa3b, v155
	v_exp_f32_e32 v155, v155
	v_pk_add_f32 v[168:169], v[168:169], 1.0 op_sel_hi:[1,0]
	v_add_f32_e32 v161, v88, v140
	v_cvt_pk_bf16_f32 v163, v164, v165
	v_add_f32_e32 v155, 1.0, v155
	v_rcp_f32_e32 v171, v155
	v_add_f32_e32 v155, v120, v136
	v_pk_mul_f32 v[166:167], v[166:167], v[170:171]
	s_nop 0
	v_pk_mul_f32 v[166:167], v[168:169], v[166:167]
	v_min_f32_e32 v168, 0x40e00000, v155
	v_mul_f32_e32 v155, 0xbfd9db23, v168
	v_mul_f32_e32 v155, 0x3fb8aa3b, v155
	v_exp_f32_e32 v155, v155
	v_med3_f32 v170, v161, s13, v222
	v_add_f32_e32 v161, v89, v141
	v_med3_f32 v171, v161, s13, v222
	v_add_f32_e32 v155, 1.0, v155
	v_rcp_f32_e32 v172, v155
	v_add_f32_e32 v155, v121, v137
	v_min_f32_e32 v169, 0x40e00000, v155
	v_mul_f32_e32 v155, 0xbfd9db23, v169
	v_mul_f32_e32 v155, 0x3fb8aa3b, v155
	v_exp_f32_e32 v155, v155
	v_pk_add_f32 v[170:171], v[170:171], 1.0 op_sel_hi:[1,0]
	v_cvt_pk_bf16_f32 v164, v166, v167
	v_add_f32_e32 v161, v82, v146
	v_add_f32_e32 v155, 1.0, v155
	v_rcp_f32_e32 v173, v155
	v_add_u32_e32 v155, 0x8000, v0
	v_pk_mul_f32 v[168:169], v[168:169], v[172:173]
	s_nop 0
	v_pk_mul_f32 v[168:169], v[170:171], v[168:169]
	s_nop 0
	v_cvt_pk_bf16_f32 v165, v168, v169
	buffer_store_dwordx4 v[162:165], v155, s[40:43], 0 offen sc1
	v_add_f32_e32 v155, v114, v142
	s_nop 0
	v_min_f32_e32 v162, 0x40e00000, v155
	v_mul_f32_e32 v155, 0xbfd9db23, v162
	v_mul_f32_e32 v155, 0x3fb8aa3b, v155
	v_exp_f32_e32 v155, v155
	v_med3_f32 v164, v161, s13, v222
	v_add_f32_e32 v161, v83, v147
	v_med3_f32 v165, v161, s13, v222
	v_add_f32_e32 v155, 1.0, v155
	v_rcp_f32_e32 v166, v155
	v_add_f32_e32 v155, v115, v143
	v_min_f32_e32 v163, 0x40e00000, v155
	v_mul_f32_e32 v155, 0xbfd9db23, v163
	v_mul_f32_e32 v155, 0x3fb8aa3b, v155
	v_exp_f32_e32 v155, v155
	v_pk_add_f32 v[164:165], v[164:165], 1.0 op_sel_hi:[1,0]
	v_add_f32_e32 v161, v84, v148
	v_add_f32_e32 v155, 1.0, v155
	v_rcp_f32_e32 v167, v155
	v_add_f32_e32 v155, v116, v144
	v_pk_mul_f32 v[162:163], v[162:163], v[166:167]
	s_nop 0
	v_pk_mul_f32 v[162:163], v[164:165], v[162:163]
	v_min_f32_e32 v164, 0x40e00000, v155
	v_mul_f32_e32 v155, 0xbfd9db23, v164
	v_mul_f32_e32 v155, 0x3fb8aa3b, v155
	v_exp_f32_e32 v155, v155
	v_med3_f32 v166, v161, s13, v222
	v_add_f32_e32 v161, v85, v149
	v_med3_f32 v167, v161, s13, v222
	v_add_f32_e32 v155, 1.0, v155
	v_rcp_f32_e32 v168, v155
	v_add_f32_e32 v155, v117, v145
	v_min_f32_e32 v165, 0x40e00000, v155
	v_mul_f32_e32 v155, 0xbfd9db23, v165
	v_mul_f32_e32 v155, 0x3fb8aa3b, v155
	v_exp_f32_e32 v155, v155
	v_pk_add_f32 v[166:167], v[166:167], 1.0 op_sel_hi:[1,0]
	v_add_f32_e32 v161, v78, v138
	v_cvt_pk_bf16_f32 v162, v162, v163
	v_add_f32_e32 v155, 1.0, v155
	v_rcp_f32_e32 v169, v155
	v_add_f32_e32 v155, v110, v134
	v_pk_mul_f32 v[164:165], v[164:165], v[168:169]
	s_nop 0
	v_pk_mul_f32 v[164:165], v[166:167], v[164:165]
	v_min_f32_e32 v166, 0x40e00000, v155
	v_mul_f32_e32 v155, 0xbfd9db23, v166
	v_mul_f32_e32 v155, 0x3fb8aa3b, v155
	v_exp_f32_e32 v155, v155
	v_med3_f32 v168, v161, s13, v222
	v_add_f32_e32 v161, v79, v139
	v_med3_f32 v169, v161, s13, v222
	v_add_f32_e32 v155, 1.0, v155
	v_rcp_f32_e32 v170, v155
	v_add_f32_e32 v155, v111, v135
	v_min_f32_e32 v167, 0x40e00000, v155
	v_mul_f32_e32 v155, 0xbfd9db23, v167
	v_mul_f32_e32 v155, 0x3fb8aa3b, v155
	v_exp_f32_e32 v155, v155
	v_pk_add_f32 v[168:169], v[168:169], 1.0 op_sel_hi:[1,0]
	v_add_f32_e32 v161, v80, v140
	v_cvt_pk_bf16_f32 v163, v164, v165
	v_add_f32_e32 v155, 1.0, v155
	v_rcp_f32_e32 v171, v155
	v_add_f32_e32 v155, v112, v136
	v_pk_mul_f32 v[166:167], v[166:167], v[170:171]
	s_nop 0
	v_pk_mul_f32 v[166:167], v[168:169], v[166:167]
	v_min_f32_e32 v168, 0x40e00000, v155
	v_mul_f32_e32 v155, 0xbfd9db23, v168
	v_mul_f32_e32 v155, 0x3fb8aa3b, v155
	v_exp_f32_e32 v155, v155
	v_med3_f32 v170, v161, s13, v222
	v_add_f32_e32 v161, v81, v141
	v_med3_f32 v171, v161, s13, v222
	v_add_f32_e32 v155, 1.0, v155
	v_rcp_f32_e32 v172, v155
	v_add_f32_e32 v155, v113, v137
	v_min_f32_e32 v169, 0x40e00000, v155
	v_mul_f32_e32 v155, 0xbfd9db23, v169
	v_mul_f32_e32 v155, 0x3fb8aa3b, v155
	v_exp_f32_e32 v155, v155
	v_pk_add_f32 v[170:171], v[170:171], 1.0 op_sel_hi:[1,0]
	v_cvt_pk_bf16_f32 v164, v166, v167
	v_add_f32_e32 v161, v74, v146
	v_add_f32_e32 v155, 1.0, v155
	v_rcp_f32_e32 v173, v155
	v_add_u32_e32 v155, 0x10000, v0
	v_pk_mul_f32 v[168:169], v[168:169], v[172:173]
	s_nop 0
	v_pk_mul_f32 v[168:169], v[170:171], v[168:169]
	s_nop 0
	v_cvt_pk_bf16_f32 v165, v168, v169
	buffer_store_dwordx4 v[162:165], v155, s[40:43], 0 offen sc1
	v_add_f32_e32 v155, v106, v142
	s_nop 0
	v_min_f32_e32 v162, 0x40e00000, v155
	v_mul_f32_e32 v155, 0xbfd9db23, v162
	v_mul_f32_e32 v155, 0x3fb8aa3b, v155
	v_exp_f32_e32 v155, v155
	v_med3_f32 v164, v161, s13, v222
	v_add_f32_e32 v161, v75, v147
	v_med3_f32 v165, v161, s13, v222
	v_add_f32_e32 v155, 1.0, v155
	v_rcp_f32_e32 v166, v155
	v_add_f32_e32 v155, v107, v143
	v_min_f32_e32 v163, 0x40e00000, v155
	v_mul_f32_e32 v155, 0xbfd9db23, v163
	v_mul_f32_e32 v155, 0x3fb8aa3b, v155
	v_exp_f32_e32 v155, v155
	v_pk_add_f32 v[164:165], v[164:165], 1.0 op_sel_hi:[1,0]
	v_add_f32_e32 v161, v76, v148
	v_add_f32_e32 v155, 1.0, v155
	v_rcp_f32_e32 v167, v155
	v_add_f32_e32 v155, v108, v144
	v_pk_mul_f32 v[162:163], v[162:163], v[166:167]
	s_nop 0
	v_pk_mul_f32 v[162:163], v[164:165], v[162:163]
	v_min_f32_e32 v164, 0x40e00000, v155
	v_mul_f32_e32 v155, 0xbfd9db23, v164
	v_mul_f32_e32 v155, 0x3fb8aa3b, v155
	v_exp_f32_e32 v155, v155
	v_med3_f32 v166, v161, s13, v222
	v_add_f32_e32 v161, v77, v149
	v_med3_f32 v167, v161, s13, v222
	v_add_f32_e32 v155, 1.0, v155
	v_rcp_f32_e32 v168, v155
	v_add_f32_e32 v155, v109, v145
	v_min_f32_e32 v165, 0x40e00000, v155
	v_mul_f32_e32 v155, 0xbfd9db23, v165
	v_mul_f32_e32 v155, 0x3fb8aa3b, v155
	v_exp_f32_e32 v155, v155
	v_pk_add_f32 v[166:167], v[166:167], 1.0 op_sel_hi:[1,0]
	v_add_f32_e32 v161, v70, v138
	v_cvt_pk_bf16_f32 v162, v162, v163
	v_add_f32_e32 v155, 1.0, v155
	v_rcp_f32_e32 v169, v155
	v_add_f32_e32 v155, v102, v134
	v_pk_mul_f32 v[164:165], v[164:165], v[168:169]
	s_nop 0
	v_pk_mul_f32 v[164:165], v[166:167], v[164:165]
	v_min_f32_e32 v166, 0x40e00000, v155
	v_mul_f32_e32 v155, 0xbfd9db23, v166
	v_mul_f32_e32 v155, 0x3fb8aa3b, v155
	v_exp_f32_e32 v155, v155
	v_med3_f32 v168, v161, s13, v222
	v_add_f32_e32 v161, v71, v139
	v_med3_f32 v169, v161, s13, v222
	v_add_f32_e32 v155, 1.0, v155
	v_rcp_f32_e32 v170, v155
	v_add_f32_e32 v155, v103, v135
	v_min_f32_e32 v167, 0x40e00000, v155
	v_mul_f32_e32 v155, 0xbfd9db23, v167
	v_mul_f32_e32 v155, 0x3fb8aa3b, v155
	v_exp_f32_e32 v155, v155
	v_pk_add_f32 v[168:169], v[168:169], 1.0 op_sel_hi:[1,0]
	v_add_f32_e32 v161, v72, v140
	v_cvt_pk_bf16_f32 v163, v164, v165
	v_add_f32_e32 v155, 1.0, v155
	v_rcp_f32_e32 v171, v155
	v_add_f32_e32 v155, v104, v136
	v_pk_mul_f32 v[166:167], v[166:167], v[170:171]
	s_nop 0
	v_pk_mul_f32 v[166:167], v[168:169], v[166:167]
	v_min_f32_e32 v168, 0x40e00000, v155
	v_mul_f32_e32 v155, 0xbfd9db23, v168
	v_mul_f32_e32 v155, 0x3fb8aa3b, v155
	v_exp_f32_e32 v155, v155
	v_med3_f32 v170, v161, s13, v222
	v_add_f32_e32 v161, v73, v141
	v_med3_f32 v171, v161, s13, v222
	v_add_f32_e32 v155, 1.0, v155
	v_rcp_f32_e32 v172, v155
	v_add_f32_e32 v155, v105, v137
	v_min_f32_e32 v169, 0x40e00000, v155
	v_mul_f32_e32 v155, 0xbfd9db23, v169
	v_mul_f32_e32 v155, 0x3fb8aa3b, v155
	v_exp_f32_e32 v155, v155
	v_pk_add_f32 v[170:171], v[170:171], 1.0 op_sel_hi:[1,0]
	v_cvt_pk_bf16_f32 v164, v166, v167
	v_add_f32_e32 v161, v30, v146
	v_add_f32_e32 v155, 1.0, v155
	v_rcp_f32_e32 v173, v155
	v_add_u32_e32 v155, 0x18000, v0
	v_pk_mul_f32 v[168:169], v[168:169], v[172:173]
	s_nop 0
	v_pk_mul_f32 v[168:169], v[170:171], v[168:169]
	s_nop 0
	v_cvt_pk_bf16_f32 v165, v168, v169
	buffer_store_dwordx4 v[162:165], v155, s[40:43], 0 offen sc1
	v_add_f32_e32 v155, v66, v142
	s_nop 0
	v_min_f32_e32 v162, 0x40e00000, v155
	v_mul_f32_e32 v155, 0xbfd9db23, v162
	v_mul_f32_e32 v155, 0x3fb8aa3b, v155
	v_exp_f32_e32 v155, v155
	v_med3_f32 v164, v161, s13, v222
	v_add_f32_e32 v161, v31, v147
	v_med3_f32 v165, v161, s13, v222
	v_add_f32_e32 v155, 1.0, v155
	v_rcp_f32_e32 v166, v155
	v_add_f32_e32 v155, v67, v143
	v_min_f32_e32 v163, 0x40e00000, v155
	v_mul_f32_e32 v155, 0xbfd9db23, v163
	v_mul_f32_e32 v155, 0x3fb8aa3b, v155
	v_exp_f32_e32 v155, v155
	v_pk_add_f32 v[164:165], v[164:165], 1.0 op_sel_hi:[1,0]
	v_add_f32_e32 v161, v32, v148
	v_add_f32_e32 v155, 1.0, v155
	v_rcp_f32_e32 v167, v155
	v_add_f32_e32 v155, v68, v144
	v_pk_mul_f32 v[162:163], v[162:163], v[166:167]
	s_nop 0
	v_pk_mul_f32 v[162:163], v[164:165], v[162:163]
	v_min_f32_e32 v164, 0x40e00000, v155
	v_mul_f32_e32 v155, 0xbfd9db23, v164
	v_mul_f32_e32 v155, 0x3fb8aa3b, v155
	v_exp_f32_e32 v155, v155
	v_med3_f32 v166, v161, s13, v222
	v_add_f32_e32 v161, v33, v149
	v_med3_f32 v167, v161, s13, v222
	v_add_f32_e32 v155, 1.0, v155
	v_rcp_f32_e32 v168, v155
	v_add_f32_e32 v155, v69, v145
	v_min_f32_e32 v165, 0x40e00000, v155
	v_mul_f32_e32 v155, 0xbfd9db23, v165
	v_mul_f32_e32 v155, 0x3fb8aa3b, v155
	v_exp_f32_e32 v155, v155
	v_pk_add_f32 v[166:167], v[166:167], 1.0 op_sel_hi:[1,0]
	v_add_f32_e32 v161, v26, v138
	v_cvt_pk_bf16_f32 v162, v162, v163
	v_add_f32_e32 v155, 1.0, v155
	v_rcp_f32_e32 v169, v155
	v_add_f32_e32 v155, v62, v134
	v_pk_mul_f32 v[164:165], v[164:165], v[168:169]
	s_nop 0
	v_pk_mul_f32 v[164:165], v[166:167], v[164:165]
	v_min_f32_e32 v166, 0x40e00000, v155
	v_mul_f32_e32 v155, 0xbfd9db23, v166
	v_mul_f32_e32 v155, 0x3fb8aa3b, v155
	v_exp_f32_e32 v155, v155
	v_med3_f32 v168, v161, s13, v222
	v_add_f32_e32 v161, v27, v139
	v_med3_f32 v169, v161, s13, v222
	v_add_f32_e32 v155, 1.0, v155
	v_rcp_f32_e32 v170, v155
	v_add_f32_e32 v155, v63, v135
	v_min_f32_e32 v167, 0x40e00000, v155
	v_mul_f32_e32 v155, 0xbfd9db23, v167
	v_mul_f32_e32 v155, 0x3fb8aa3b, v155
	v_exp_f32_e32 v155, v155
	v_pk_add_f32 v[168:169], v[168:169], 1.0 op_sel_hi:[1,0]
	v_add_f32_e32 v161, v28, v140
	v_cvt_pk_bf16_f32 v163, v164, v165
	v_add_f32_e32 v155, 1.0, v155
	v_rcp_f32_e32 v171, v155
	v_add_f32_e32 v155, v64, v136
	v_pk_mul_f32 v[166:167], v[166:167], v[170:171]
	s_nop 0
	v_pk_mul_f32 v[166:167], v[168:169], v[166:167]
	v_min_f32_e32 v168, 0x40e00000, v155
	v_mul_f32_e32 v155, 0xbfd9db23, v168
	v_mul_f32_e32 v155, 0x3fb8aa3b, v155
	v_exp_f32_e32 v155, v155
	v_med3_f32 v170, v161, s13, v222
	v_add_f32_e32 v161, v29, v141
	v_med3_f32 v171, v161, s13, v222
	v_add_f32_e32 v155, 1.0, v155
	v_rcp_f32_e32 v172, v155
	v_add_f32_e32 v155, v65, v137
	v_min_f32_e32 v169, 0x40e00000, v155
	v_mul_f32_e32 v155, 0xbfd9db23, v169
	v_mul_f32_e32 v155, 0x3fb8aa3b, v155
	v_exp_f32_e32 v155, v155
	v_pk_add_f32 v[170:171], v[170:171], 1.0 op_sel_hi:[1,0]
	v_cvt_pk_bf16_f32 v164, v166, v167
	v_add_f32_e32 v161, v22, v146
	v_add_f32_e32 v155, 1.0, v155
	v_rcp_f32_e32 v173, v155
	v_add_u32_e32 v155, 0x40000, v0
	v_pk_mul_f32 v[168:169], v[168:169], v[172:173]
	s_nop 0
	v_pk_mul_f32 v[168:169], v[170:171], v[168:169]
	s_nop 0
	v_cvt_pk_bf16_f32 v165, v168, v169
	buffer_store_dwordx4 v[162:165], v155, s[40:43], 0 offen sc1
	v_add_f32_e32 v155, v58, v142
	s_nop 0
	v_min_f32_e32 v162, 0x40e00000, v155
	v_mul_f32_e32 v155, 0xbfd9db23, v162
	v_mul_f32_e32 v155, 0x3fb8aa3b, v155
	v_exp_f32_e32 v155, v155
	v_med3_f32 v164, v161, s13, v222
	v_add_f32_e32 v161, v23, v147
	v_med3_f32 v165, v161, s13, v222
	v_add_f32_e32 v155, 1.0, v155
	v_rcp_f32_e32 v166, v155
	v_add_f32_e32 v155, v59, v143
	v_min_f32_e32 v163, 0x40e00000, v155
	v_mul_f32_e32 v155, 0xbfd9db23, v163
	v_mul_f32_e32 v155, 0x3fb8aa3b, v155
	v_exp_f32_e32 v155, v155
	v_pk_add_f32 v[164:165], v[164:165], 1.0 op_sel_hi:[1,0]
	v_add_f32_e32 v161, v24, v148
	v_add_f32_e32 v155, 1.0, v155
	v_rcp_f32_e32 v167, v155
	v_add_f32_e32 v155, v60, v144
	v_pk_mul_f32 v[162:163], v[162:163], v[166:167]
	s_nop 0
	v_pk_mul_f32 v[162:163], v[164:165], v[162:163]
	v_min_f32_e32 v164, 0x40e00000, v155
	v_mul_f32_e32 v155, 0xbfd9db23, v164
	v_mul_f32_e32 v155, 0x3fb8aa3b, v155
	v_exp_f32_e32 v155, v155
	v_med3_f32 v166, v161, s13, v222
	v_add_f32_e32 v161, v25, v149
	v_med3_f32 v167, v161, s13, v222
	v_add_f32_e32 v155, 1.0, v155
	v_rcp_f32_e32 v168, v155
	v_add_f32_e32 v155, v61, v145
	v_min_f32_e32 v165, 0x40e00000, v155
	v_mul_f32_e32 v155, 0xbfd9db23, v165
	v_mul_f32_e32 v155, 0x3fb8aa3b, v155
	v_exp_f32_e32 v155, v155
	v_pk_add_f32 v[166:167], v[166:167], 1.0 op_sel_hi:[1,0]
	v_add_f32_e32 v161, v18, v138
	v_cvt_pk_bf16_f32 v162, v162, v163
	v_add_f32_e32 v155, 1.0, v155
	v_rcp_f32_e32 v169, v155
	v_add_f32_e32 v155, v54, v134
	v_pk_mul_f32 v[164:165], v[164:165], v[168:169]
	s_nop 0
	v_pk_mul_f32 v[164:165], v[166:167], v[164:165]
	v_min_f32_e32 v166, 0x40e00000, v155
	v_mul_f32_e32 v155, 0xbfd9db23, v166
	v_mul_f32_e32 v155, 0x3fb8aa3b, v155
	v_exp_f32_e32 v155, v155
	v_med3_f32 v168, v161, s13, v222
	v_add_f32_e32 v161, v19, v139
	v_med3_f32 v169, v161, s13, v222
	v_add_f32_e32 v155, 1.0, v155
	v_rcp_f32_e32 v170, v155
	v_add_f32_e32 v155, v55, v135
	v_min_f32_e32 v167, 0x40e00000, v155
	v_mul_f32_e32 v155, 0xbfd9db23, v167
	v_mul_f32_e32 v155, 0x3fb8aa3b, v155
	v_exp_f32_e32 v155, v155
	v_pk_add_f32 v[168:169], v[168:169], 1.0 op_sel_hi:[1,0]
	v_add_f32_e32 v161, v20, v140
	v_cvt_pk_bf16_f32 v163, v164, v165
	v_add_f32_e32 v155, 1.0, v155
	v_rcp_f32_e32 v171, v155
	v_add_f32_e32 v155, v56, v136
	v_pk_mul_f32 v[166:167], v[166:167], v[170:171]
	s_nop 0
	v_pk_mul_f32 v[166:167], v[168:169], v[166:167]
	v_min_f32_e32 v168, 0x40e00000, v155
	v_mul_f32_e32 v155, 0xbfd9db23, v168
	v_mul_f32_e32 v155, 0x3fb8aa3b, v155
	v_exp_f32_e32 v155, v155
	v_med3_f32 v170, v161, s13, v222
	v_add_f32_e32 v161, v21, v141
	v_med3_f32 v171, v161, s13, v222
	v_add_f32_e32 v155, 1.0, v155
	v_rcp_f32_e32 v172, v155
	v_add_f32_e32 v155, v57, v137
	v_min_f32_e32 v169, 0x40e00000, v155
	v_mul_f32_e32 v155, 0xbfd9db23, v169
	v_mul_f32_e32 v155, 0x3fb8aa3b, v155
	v_exp_f32_e32 v155, v155
	v_pk_add_f32 v[170:171], v[170:171], 1.0 op_sel_hi:[1,0]
	v_cvt_pk_bf16_f32 v164, v166, v167
	v_add_f32_e32 v161, v14, v146
	v_add_f32_e32 v155, 1.0, v155
	v_rcp_f32_e32 v173, v155
	v_add_u32_e32 v155, 0x48000, v0
	v_add_f32_e32 v146, v6, v146
	v_med3_f32 v146, v146, s13, v222
	v_pk_mul_f32 v[168:169], v[168:169], v[172:173]
	s_nop 0
	v_pk_mul_f32 v[168:169], v[170:171], v[168:169]
	s_nop 0
	v_cvt_pk_bf16_f32 v165, v168, v169
	buffer_store_dwordx4 v[162:165], v155, s[40:43], 0 offen sc1
	v_add_f32_e32 v155, v50, v142
	v_add_f32_e32 v142, v42, v142
	v_min_f32_e32 v162, 0x40e00000, v155
	v_mul_f32_e32 v155, 0xbfd9db23, v162
	v_mul_f32_e32 v155, 0x3fb8aa3b, v155
	v_exp_f32_e32 v155, v155
	v_med3_f32 v164, v161, s13, v222
	v_add_f32_e32 v161, v15, v147
	v_med3_f32 v165, v161, s13, v222
	v_add_f32_e32 v155, 1.0, v155
	v_rcp_f32_e32 v166, v155
	v_add_f32_e32 v155, v51, v143
	v_min_f32_e32 v163, 0x40e00000, v155
	v_mul_f32_e32 v155, 0xbfd9db23, v163
	v_mul_f32_e32 v155, 0x3fb8aa3b, v155
	v_exp_f32_e32 v155, v155
	v_pk_add_f32 v[164:165], v[164:165], 1.0 op_sel_hi:[1,0]
	v_add_f32_e32 v161, v16, v148
	v_min_f32_e32 v142, 0x40e00000, v142
	v_add_f32_e32 v155, 1.0, v155
	v_rcp_f32_e32 v167, v155
	v_add_f32_e32 v155, v52, v144
	v_add_f32_e32 v143, v43, v143
	v_min_f32_e32 v143, 0x40e00000, v143
	v_pk_mul_f32 v[162:163], v[162:163], v[166:167]
	v_med3_f32 v166, v161, s13, v222
	v_pk_mul_f32 v[162:163], v[164:165], v[162:163]
	v_min_f32_e32 v164, 0x40e00000, v155
	v_mul_f32_e32 v155, 0xbfd9db23, v164
	v_mul_f32_e32 v155, 0x3fb8aa3b, v155
	v_exp_f32_e32 v155, v155
	v_add_f32_e32 v161, v17, v149
	v_med3_f32 v167, v161, s13, v222
	v_pk_add_f32 v[166:167], v[166:167], 1.0 op_sel_hi:[1,0]
	v_add_f32_e32 v155, 1.0, v155
	v_rcp_f32_e32 v168, v155
	v_add_f32_e32 v155, v53, v145
	v_min_f32_e32 v165, 0x40e00000, v155
	v_mul_f32_e32 v155, 0xbfd9db23, v165
	v_mul_f32_e32 v155, 0x3fb8aa3b, v155
	v_exp_f32_e32 v155, v155
	v_add_f32_e32 v161, v10, v138
	v_cvt_pk_bf16_f32 v162, v162, v163
	v_add_f32_e32 v147, v7, v147
	v_add_f32_e32 v155, 1.0, v155
	v_rcp_f32_e32 v169, v155
	v_add_f32_e32 v155, v46, v134
	v_med3_f32 v147, v147, s13, v222
	v_add_f32_e32 v144, v44, v144
	v_pk_mul_f32 v[164:165], v[164:165], v[168:169]
	v_med3_f32 v168, v161, s13, v222
	v_pk_mul_f32 v[164:165], v[166:167], v[164:165]
	v_min_f32_e32 v166, 0x40e00000, v155
	v_mul_f32_e32 v155, 0xbfd9db23, v166
	v_mul_f32_e32 v155, 0x3fb8aa3b, v155
	v_exp_f32_e32 v155, v155
	v_add_f32_e32 v161, v11, v139
	v_med3_f32 v169, v161, s13, v222
	v_pk_add_f32 v[168:169], v[168:169], 1.0 op_sel_hi:[1,0]
	v_add_f32_e32 v155, 1.0, v155
	v_rcp_f32_e32 v170, v155
	v_add_f32_e32 v155, v47, v135
	v_min_f32_e32 v167, 0x40e00000, v155
	v_mul_f32_e32 v155, 0xbfd9db23, v167
	v_mul_f32_e32 v155, 0x3fb8aa3b, v155
	v_exp_f32_e32 v155, v155
	v_add_f32_e32 v161, v12, v140
	v_cvt_pk_bf16_f32 v163, v164, v165
	v_pk_add_f32 v[146:147], v[146:147], 1.0 op_sel_hi:[1,0]
	v_add_f32_e32 v155, 1.0, v155
	v_rcp_f32_e32 v171, v155
	v_add_f32_e32 v155, v48, v136
	v_min_f32_e32 v144, 0x40e00000, v144
	v_add_f32_e32 v145, v45, v145
	v_pk_mul_f32 v[166:167], v[166:167], v[170:171]
	v_med3_f32 v170, v161, s13, v222
	v_pk_mul_f32 v[166:167], v[168:169], v[166:167]
	v_min_f32_e32 v168, 0x40e00000, v155
	v_mul_f32_e32 v155, 0xbfd9db23, v168
	v_mul_f32_e32 v155, 0x3fb8aa3b, v155
	v_exp_f32_e32 v155, v155
	v_add_f32_e32 v161, v13, v141
	v_med3_f32 v171, v161, s13, v222
	v_pk_add_f32 v[170:171], v[170:171], 1.0 op_sel_hi:[1,0]
	v_add_f32_e32 v155, 1.0, v155
	v_rcp_f32_e32 v172, v155
	v_add_f32_e32 v155, v49, v137
	v_min_f32_e32 v169, 0x40e00000, v155
	v_mul_f32_e32 v155, 0xbfd9db23, v169
	v_mul_f32_e32 v155, 0x3fb8aa3b, v155
	v_exp_f32_e32 v155, v155
	v_cvt_pk_bf16_f32 v164, v166, v167
	v_min_f32_e32 v145, 0x40e00000, v145
	v_add_f32_e32 v134, v38, v134
	v_add_f32_e32 v155, 1.0, v155
	v_rcp_f32_e32 v173, v155
	v_add_u32_e32 v155, 0x50000, v0
	v_add_f32_e32 v135, v39, v135
	v_min_f32_e32 v134, 0x40e00000, v134
	v_pk_mul_f32 v[168:169], v[168:169], v[172:173]
	v_min_f32_e32 v135, 0x40e00000, v135
	v_pk_mul_f32 v[168:169], v[170:171], v[168:169]
	v_add_f32_e32 v138, v2, v138
	v_cvt_pk_bf16_f32 v165, v168, v169
	buffer_store_dwordx4 v[162:165], v155, s[40:43], 0 offen sc1
	v_mul_f32_e32 v155, 0xbfd9db23, v142
	v_mul_f32_e32 v155, 0x3fb8aa3b, v155
	v_exp_f32_e32 v155, v155
	v_add_f32_e32 v139, v3, v139
	v_med3_f32 v138, v138, s13, v222
	v_med3_f32 v139, v139, s13, v222
	v_add_f32_e32 v155, 1.0, v155
	v_rcp_f32_e32 v162, v155
	v_mul_f32_e32 v155, 0xbfd9db23, v143
	v_mul_f32_e32 v155, 0x3fb8aa3b, v155
	v_exp_f32_e32 v155, v155
	v_pk_add_f32 v[138:139], v[138:139], 1.0 op_sel_hi:[1,0]
	v_add_u32_e32 v0, 0x58000, v0
	v_add_f32_e32 v155, 1.0, v155
	v_rcp_f32_e32 v163, v155
	s_nop 0
	v_pk_mul_f32 v[142:143], v[142:143], v[162:163]
	s_nop 0
	v_pk_mul_f32 v[142:143], v[146:147], v[142:143]
	v_mul_f32_e32 v147, 0xbfd9db23, v144
	v_mul_f32_e32 v147, 0x3fb8aa3b, v147
	v_exp_f32_e32 v147, v147
	v_add_f32_e32 v146, v8, v148
	v_med3_f32 v146, v146, s13, v222
	v_add_f32_e32 v147, 1.0, v147
	v_rcp_f32_e32 v148, v147
	v_add_f32_e32 v147, v9, v149
	v_mul_f32_e32 v149, 0xbfd9db23, v145
	v_mul_f32_e32 v149, 0x3fb8aa3b, v149
	v_exp_f32_e32 v149, v149
	v_med3_f32 v147, v147, s13, v222
	v_pk_add_f32 v[146:147], v[146:147], 1.0 op_sel_hi:[1,0]
	v_add_f32_e32 v149, 1.0, v149
	v_rcp_f32_e32 v149, v149
	s_nop 0
	v_pk_mul_f32 v[144:145], v[144:145], v[148:149]
	s_nop 0
	v_pk_mul_f32 v[144:145], v[146:147], v[144:145]
	v_mul_f32_e32 v146, 0xbfd9db23, v134
	v_mul_f32_e32 v147, 0xbfd9db23, v135
	v_mul_f32_e32 v146, 0x3fb8aa3b, v146
	v_mul_f32_e32 v147, 0x3fb8aa3b, v147
	v_exp_f32_e32 v146, v146
	v_exp_f32_e32 v147, v147
	v_add_f32_e32 v146, 1.0, v146
	v_add_f32_e32 v147, 1.0, v147
	v_rcp_f32_e32 v146, v146
	v_rcp_f32_e32 v147, v147
	s_nop 0
	v_pk_mul_f32 v[134:135], v[134:135], v[146:147]
	s_nop 0
	v_pk_mul_f32 v[138:139], v[138:139], v[134:135]
	v_add_f32_e32 v134, v40, v136
	v_add_f32_e32 v135, v4, v140
	v_min_f32_e32 v134, 0x40e00000, v134
	v_med3_f32 v136, v135, s13, v222
	v_mul_f32_e32 v135, 0xbfd9db23, v134
	v_mul_f32_e32 v135, 0x3fb8aa3b, v135
	v_exp_f32_e32 v135, v135
	s_nop 0
	v_add_f32_e32 v135, 1.0, v135
	v_rcp_f32_e32 v140, v135
	v_add_f32_e32 v135, v41, v137
	v_min_f32_e32 v135, 0x40e00000, v135
	v_add_f32_e32 v137, v5, v141
	v_mul_f32_e32 v141, 0xbfd9db23, v135
	v_mul_f32_e32 v141, 0x3fb8aa3b, v141
	v_exp_f32_e32 v141, v141
	v_med3_f32 v137, v137, s13, v222
	v_pk_add_f32 v[136:137], v[136:137], 1.0 op_sel_hi:[1,0]
	v_add_f32_e32 v141, 1.0, v141
	v_rcp_f32_e32 v141, v141
	s_nop 0
	v_pk_mul_f32 v[134:135], v[134:135], v[140:141]
	s_nop 0
	v_pk_mul_f32 v[140:141], v[136:137], v[134:135]
	v_cvt_pk_bf16_f32 v134, v142, v143
	v_cvt_pk_bf16_f32 v135, v144, v145
	v_cvt_pk_bf16_f32 v136, v138, v139
	v_cvt_pk_bf16_f32 v137, v140, v141
	buffer_store_dwordx4 v[134:137], v0, s[40:43], 0 offen sc1
	s_add_u32 s42, s29, 0xffffff00
	s_addc_u32 s43, s31, -1
	s_and_b64 vcc, exec, s[0:1]
	s_cbranch_vccz .LBB0_2070

.LBB0_2081:
	s_waitcnt vmcnt(0)
	v_mov_b32_e32 v34, 0
	v_mov_b32_e32 v35, 0
	v_mov_b32_e32 v36, 0
	v_mov_b32_e32 v37, 0
	v_mov_b32_e32 v204, 1
	v_mov_b32_e32 v205, 0xbf3a00e3
	v_mov_b32_e32 v206, 0x3727c5ac
	v_mov_b32_e32 v207, 0x260
	v_mov_b32_e32 v208, 0x3a27c5ac
	v_mov_b32_e32 v212, 0x1c00
	v_mov_b32_e32 v213, 0x80
	v_mov_b32_e32 v214, 0x180
	v_mov_b32_e32 v215, 0x37160000
	v_mov_b32_e32 v216, 14
	v_mov_b32_e32 v217, 0x2400
	s_cmp_gt_i32 s50, -1
	s_cselect_b64 s[0:1], -1, 0
	s_and_b64 s[2:3], s[4:5], s[0:1]
	s_barrier
	s_and_saveexec_b64 s[0:1], s[2:3]
	s_cbranch_execz .LBB0_2084
	s_mov_b64 s[2:3], exec
	v_mbcnt_lo_u32_b32 v0, s2, 0
	v_mbcnt_hi_u32_b32 v0, s3, v0
	v_cmp_eq_u32_e32 vcc, 0, v0
	s_and_b64 s[4:5], exec, vcc
	s_mov_b64 exec, s[4:5]
	s_cbranch_execz .LBB0_2084
	v_readlane_b32 s4, v253, 54
	v_readlane_b32 s5, v253, 55
	s_mov_b32 s51, s4
	s_lshl_b64 s[4:5], s[50:51], 2
	s_add_u32 s4, s14, s4
	s_addc_u32 s5, s15, s5
	s_bcnt1_i32_b64 s2, s[2:3]
	v_mov_b32_e32 v0, s2
	global_atomic_add v1, v0, s[4:5]
	v_readlane_b32 s6, v253, 56
	v_readlane_b32 s7, v253, 57
